# speedup vs baseline: 1.0046x; 1.0046x over previous
_Z7k_stageILi0ELi8EEv8AttnArgsPKDF16_PKfPDF16_iii:
	s_load_dwordx16 s[64:79], s[0:1], 0x40
	s_load_dwordx16 s[64:79], s[0:1], 0x0
	v_readfirstlane_b32 s94, v0
	s_nop 0
	s_lshr_b32 s94, s94, 6
	s_cmp_ge_u32 s94, 4
	s_cbranch_scc1 .Lmyprio3
	s_setprio 1

_Z7k_stageILi1ELi4EEv8AttnArgsPKDF16_PKfPDF16_iii:
	s_load_dwordx16 s[64:79], s[0:1], 0x0
	v_readfirstlane_b32 s94, v0
	s_nop 0
	s_lshr_b32 s94, s94, 6
	s_cmp_ge_u32 s94, 4
	s_cbranch_scc1 .Lmyprio4
	s_setprio 1
